# NA main loop: position-bias LDS reads issued at the top of the iteration instead of behind the QK MFMAs
# baseline (speedup 1.0000x reference)
.LBB0_469:
	s_add_i32 s72, s2, s92
	v_med3_i32 v239, s72, -7, 7
	v_lshlrev_b32_e32 v239, 7, v239
	v_lshl_add_u32 v239, v183, 2, v239
	v_add_u32_e32 v239, 0x10bbc, v239
	ds_read2_b32 v[206:207], v239 offset0:0 offset1:32
	ds_read2_b32 v[208:209], v239 offset0:1 offset1:33
	ds_read2_b32 v[210:211], v239 offset0:2 offset1:34
	ds_read2_b32 v[212:213], v239 offset0:3 offset1:35
	ds_read2_b32 v[214:215], v239 offset0:8 offset1:40
	ds_read2_b32 v[216:217], v239 offset0:9 offset1:41
	ds_read2_b32 v[218:219], v239 offset0:10 offset1:42
	ds_read2_b32 v[220:221], v239 offset0:11 offset1:43
	ds_read2_b32 v[222:223], v239 offset0:16 offset1:48
	ds_read2_b32 v[224:225], v239 offset0:17 offset1:49
	ds_read2_b32 v[226:227], v239 offset0:18 offset1:50
	ds_read2_b32 v[228:229], v239 offset0:19 offset1:51
	ds_read2_b32 v[230:231], v239 offset0:24 offset1:56
	ds_read2_b32 v[232:233], v239 offset0:25 offset1:57
	ds_read2_b32 v[234:235], v239 offset0:26 offset1:58
	s_waitcnt lgkmcnt(14)
	ds_read2_b32 v[236:237], v239 offset0:27 offset1:59
	v_mov_b32_e32 v238, 0xff800000
	v_lshl_add_u64 v[66:67], v[154:155], 0, s[96:97]
	v_add_co_u32_e32 v70, vcc, 0x52002000, v66
	v_lshl_add_u64 v[68:69], v[156:157], 0, s[96:97]
	s_nop 0
	v_addc_co_u32_e32 v71, vcc, 0, v67, vcc
	global_load_dwordx2 v[164:165], v[70:71], off
	v_add_co_u32_e32 v70, vcc, 0x52002000, v68
	s_and_b32 s1, s3, 0x4000
	s_nop 0
	v_addc_co_u32_e32 v71, vcc, 0, v69, vcc
	v_add_co_u32_e32 v66, vcc, 0x4e002000, v66
	global_load_dwordx2 v[162:163], v[70:71], off
	s_nop 0
	v_addc_co_u32_e32 v67, vcc, 0, v67, vcc
	global_load_dwordx2 v[160:161], v[66:67], off
	v_add_co_u32_e32 v66, vcc, 0x4e002000, v68
	s_add_i32 s72, s1, 0
	s_nop 0
	v_addc_co_u32_e32 v67, vcc, 0, v69, vcc
	v_add3_u32 v0, s72, v199, v189
	v_add3_u32 v98, s72, v197, v189
	global_load_dwordx2 v[158:159], v[66:67], off
	s_cmp_lt_u32 s92, s84
	s_cbranch_scc1 .Lna_skip
	s_cmp_ge_u32 s92, s88
	s_cbranch_scc1 .Lna_skip
	v_add_u32_e32 v0, s72, v189
	s_waitcnt lgkmcnt(6)
	v_add_u32_e32 v66, v0, v199
	ds_read_b128 v[66:69], v66 offset:32768
	v_add_u32_e32 v70, v0, v199
	ds_read_b128 v[70:73], v70 offset:40960
	v_add_u32_e32 v98, v0, v197
	ds_read_b128 v[98:101], v98 offset:32768
	v_add_u32_e32 v102, v0, v197
	ds_read_b128 v[102:105], v102 offset:40960
	v_add_u32_e32 v106, v0, v195
	ds_read_b128 v[106:109], v106 offset:32768
	v_add_u32_e32 v110, v0, v195
	ds_read_b128 v[110:113], v110 offset:40960
	v_add_u32_e32 v240, v0, v194
	ds_read_b128 v[240:243], v240 offset:32768
	v_add_u32_e32 v244, v0, v194
	ds_read_b128 v[244:247], v244 offset:40960
	v_add_u32_e32 v248, v0, v193
	ds_read_b128 v[248:251], v248 offset:32768
	s_waitcnt lgkmcnt(8)
	v_mfma_f32_32x32x16_bf16 v[82:97], v[66:69], v[114:117], 0
	s_waitcnt lgkmcnt(7)
	v_mfma_f32_32x32x16_bf16 v[66:81], v[70:73], v[114:117], 0
	s_waitcnt lgkmcnt(6)
	v_mfma_f32_32x32x16_bf16 v[82:97], v[98:101], v[118:121], v[82:97]
	v_add_u32_e32 v98, v0, v193
	ds_read_b128 v[98:101], v98 offset:40960
	s_waitcnt lgkmcnt(6)
	v_mfma_f32_32x32x16_bf16 v[66:81], v[102:105], v[118:121], v[66:81]
	v_add_u32_e32 v102, v0, v192
	ds_read_b128 v[102:105], v102 offset:32768
	s_waitcnt lgkmcnt(6)
	v_mfma_f32_32x32x16_bf16 v[82:97], v[106:109], v[122:125], v[82:97]
	v_add_u32_e32 v106, v0, v192
	ds_read_b128 v[106:109], v106 offset:40960
	s_waitcnt lgkmcnt(6)
	v_mfma_f32_32x32x16_bf16 v[66:81], v[110:113], v[122:125], v[66:81]
	v_add_u32_e32 v110, v0, v191
	ds_read_b128 v[110:113], v110 offset:32768
	s_waitcnt lgkmcnt(6)
	v_mfma_f32_32x32x16_bf16 v[82:97], v[240:243], v[126:129], v[82:97]
	v_add_u32_e32 v240, v0, v191
	ds_read_b128 v[240:243], v240 offset:40960
	s_waitcnt lgkmcnt(6)
	v_mfma_f32_32x32x16_bf16 v[66:81], v[244:247], v[126:129], v[66:81]
	v_add_u32_e32 v244, v0, v190
	ds_read_b128 v[244:247], v244 offset:32768
	s_waitcnt lgkmcnt(6)
	v_mfma_f32_32x32x16_bf16 v[82:97], v[248:251], v[130:133], v[82:97]
	v_add_u32_e32 v248, v0, v190
	ds_read_b128 v[248:251], v248 offset:40960
	s_waitcnt lgkmcnt(6)
	v_mfma_f32_32x32x16_bf16 v[66:81], v[98:101], v[130:133], v[66:81]
	s_waitcnt lgkmcnt(5)
	v_mfma_f32_32x32x16_bf16 v[82:97], v[102:105], v[134:137], v[82:97]
	s_waitcnt lgkmcnt(4)
	v_mfma_f32_32x32x16_bf16 v[66:81], v[106:109], v[134:137], v[66:81]
	s_waitcnt lgkmcnt(3)
	v_mfma_f32_32x32x16_bf16 v[82:97], v[110:113], v[138:141], v[82:97]
	s_waitcnt lgkmcnt(2)
	v_mfma_f32_32x32x16_bf16 v[66:81], v[240:243], v[138:141], v[66:81]
	s_waitcnt lgkmcnt(1)
	v_mfma_f32_32x32x16_bf16 v[82:97], v[244:247], v[142:145], v[82:97]
	s_waitcnt lgkmcnt(0)
	v_mfma_f32_32x32x16_bf16 v[66:81], v[248:251], v[142:145], v[66:81]
	s_nop 11
	s_waitcnt lgkmcnt(0)
	v_add_f32_e32 v206, v82, v206
	v_add_f32_e32 v207, v66, v207
	v_cndmask_b32_e64 v82, v238, v206, s[70:71]
	v_cndmask_b32_e64 v0, v238, v207, s[68:69]
	v_add_f32_e32 v208, v83, v208
	v_add_f32_e32 v209, v67, v209
	v_cndmask_b32_e64 v83, v238, v208, s[66:67]
	v_cndmask_b32_e64 v66, v238, v209, s[64:65]
	v_add_f32_e32 v210, v84, v210
	v_add_f32_e32 v211, v68, v211
	v_cndmask_b32_e64 v84, v238, v210, s[62:63]
	v_cndmask_b32_e64 v67, v238, v211, s[60:61]
	v_add_f32_e32 v212, v85, v212
	v_add_f32_e32 v213, v69, v213
	v_cndmask_b32_e64 v85, v238, v212, s[58:59]
	v_cndmask_b32_e64 v68, v238, v213, s[56:57]
	v_add_f32_e32 v214, v86, v214
	v_add_f32_e32 v215, v70, v215
	v_cndmask_b32_e64 v86, v238, v214, s[54:55]
	v_cndmask_b32_e64 v69, v238, v215, s[52:53]
	v_add_f32_e32 v216, v87, v216
	v_add_f32_e32 v217, v71, v217
	v_cndmask_b32_e64 v87, v238, v216, s[50:51]
	v_cndmask_b32_e64 v70, v238, v217, s[48:49]
	v_add_f32_e32 v218, v88, v218
	v_add_f32_e32 v219, v72, v219
	v_cndmask_b32_e64 v88, v238, v218, s[46:47]
	v_cndmask_b32_e64 v71, v238, v219, s[44:45]
	v_add_f32_e32 v220, v89, v220
	v_add_f32_e32 v221, v73, v221
	v_cndmask_b32_e64 v89, v238, v220, s[42:43]
	v_cndmask_b32_e64 v72, v238, v221, s[40:41]
	v_add_f32_e32 v222, v90, v222
	v_add_f32_e32 v223, v74, v223
	v_cndmask_b32_e64 v90, v238, v222, s[38:39]
	v_cndmask_b32_e64 v73, v238, v223, s[36:37]
	v_add_f32_e32 v224, v91, v224
	v_add_f32_e32 v225, v75, v225
	v_cndmask_b32_e64 v91, v238, v224, s[34:35]
	v_cndmask_b32_e64 v74, v238, v225, s[30:31]
	v_add_f32_e32 v226, v92, v226
	v_add_f32_e32 v227, v76, v227
	v_cndmask_b32_e64 v92, v238, v226, s[28:29]
	v_cndmask_b32_e64 v75, v238, v227, s[26:27]
	v_add_f32_e32 v228, v93, v228
	v_add_f32_e32 v229, v77, v229
	v_cndmask_b32_e64 v93, v238, v228, s[24:25]
	v_cndmask_b32_e64 v76, v238, v229, s[22:23]
	v_add_f32_e32 v230, v94, v230
	v_add_f32_e32 v231, v78, v231
	v_cndmask_b32_e64 v94, v238, v230, s[20:21]
	v_cndmask_b32_e64 v77, v238, v231, s[18:19]
	v_add_f32_e32 v232, v95, v232
	v_add_f32_e32 v233, v79, v233
	v_cndmask_b32_e64 v95, v238, v232, s[16:17]
	v_cndmask_b32_e64 v78, v238, v233, s[14:15]
	v_add_f32_e32 v234, v96, v234
	v_add_f32_e32 v235, v80, v235
	v_cndmask_b32_e64 v96, v238, v234, s[12:13]
	v_cndmask_b32_e64 v79, v238, v235, s[10:11]
	v_add_f32_e32 v236, v97, v236
	v_add_f32_e32 v237, v81, v237
	v_cndmask_b32_e64 v97, v238, v236, s[8:9]
	v_cndmask_b32_e64 v80, v238, v237, s[6:7]
